# speedup vs baseline: 1.0422x; 1.0001x over previous
.Lgp_wj:
	s_barrier
	ds_read_b128 v[178:181], v236 offset:28672
	ds_read_b128 v[186:189], v236 offset:30720
	ds_read_b128 v[174:177], v236 offset:32768
	ds_read_b128 v[182:185], v236 offset:34816
	ds_read_b128 v[146:149], v234
	ds_read_b128 v[150:153], v234 offset:2048
	ds_read_b128 v[154:157], v234 offset:4096
	ds_read_b128 v[158:161], v234 offset:6144
	ds_read_b128 v[162:165], v234 offset:8192
	ds_read_b128 v[166:169], v234 offset:10240
	ds_read_b128 v[170:173], v234 offset:12288
	ds_read_b128 v[218:221], v237 offset:28672
	ds_read_b128 v[222:225], v237 offset:30720
	ds_read_b128 v[226:229], v237 offset:32768
	ds_read_b128 v[230:233], v237 offset:34816
	ds_read_b128 v[190:193], v235
	ds_read_b128 v[194:197], v235 offset:2048
	ds_read_b128 v[198:201], v235 offset:4096
	ds_read_b128 v[202:205], v235 offset:6144
	ds_read_b128 v[206:209], v235 offset:8192
	ds_read_b128 v[210:213], v235 offset:10240
	ds_read_b128 v[214:217], v235 offset:12288
	s_waitcnt lgkmcnt(11)
	v_mfma_f32_16x16x32_f16 v[110:113], v[146:149], v[178:181], v[110:113]
	v_mfma_f32_16x16x32_f16 v[106:109], v[146:149], v[186:189], v[106:109]
	v_mfma_f32_16x16x32_f16 v[50:53], v[146:149], v[174:177], v[50:53]
	v_mfma_f32_16x16x32_f16 v[54:57], v[146:149], v[182:185], v[54:57]
	v_mfma_f32_16x16x32_f16 v[98:101], v[150:153], v[178:181], v[98:101]
	v_mfma_f32_16x16x32_f16 v[102:105], v[150:153], v[186:189], v[102:105]
	v_mfma_f32_16x16x32_f16 v[42:45], v[150:153], v[174:177], v[42:45]
	v_mfma_f32_16x16x32_f16 v[46:49], v[150:153], v[182:185], v[46:49]
	v_mfma_f32_16x16x32_f16 v[90:93], v[154:157], v[178:181], v[90:93]
	v_mfma_f32_16x16x32_f16 v[94:97], v[154:157], v[186:189], v[94:97]
	v_mfma_f32_16x16x32_f16 v[34:37], v[154:157], v[174:177], v[34:37]
	v_mfma_f32_16x16x32_f16 v[38:41], v[154:157], v[182:185], v[38:41]
	v_mfma_f32_16x16x32_f16 v[82:85], v[158:161], v[178:181], v[82:85]
	v_mfma_f32_16x16x32_f16 v[86:89], v[158:161], v[186:189], v[86:89]
	v_mfma_f32_16x16x32_f16 v[18:21], v[158:161], v[174:177], v[18:21]
	v_mfma_f32_16x16x32_f16 v[22:25], v[158:161], v[182:185], v[22:25]
	v_mfma_f32_16x16x32_f16 v[74:77], v[162:165], v[178:181], v[74:77]
	v_mfma_f32_16x16x32_f16 v[78:81], v[162:165], v[186:189], v[78:81]
	v_mfma_f32_16x16x32_f16 v[10:13], v[162:165], v[174:177], v[10:13]
	v_mfma_f32_16x16x32_f16 v[14:17], v[162:165], v[182:185], v[14:17]
	v_mfma_f32_16x16x32_f16 v[66:69], v[166:169], v[178:181], v[66:69]
	v_mfma_f32_16x16x32_f16 v[70:73], v[166:169], v[186:189], v[70:73]
	v_mfma_f32_16x16x32_f16 v[2:5], v[166:169], v[174:177], v[2:5]
	v_mfma_f32_16x16x32_f16 v[6:9], v[166:169], v[182:185], v[6:9]
	v_mfma_f32_16x16x32_f16 v[58:61], v[170:173], v[178:181], v[58:61]
	v_mfma_f32_16x16x32_f16 v[62:65], v[170:173], v[186:189], v[62:65]
	v_mfma_f32_16x16x32_f16 v[26:29], v[170:173], v[174:177], v[26:29]
	v_mfma_f32_16x16x32_f16 v[30:33], v[170:173], v[182:185], v[30:33]
	s_waitcnt lgkmcnt(0)
	s_waitcnt vmcnt(0)
	s_barrier
	s_cmp_eq_u32 s92, 0
	s_cbranch_scc1 .Lgp_classB
	.p2alignl 6, 3212836864

.Lgp_skip_3:
	v_lshl_add_u64 v[132:133], v[132:133], 0, s[0:1]
	v_mfma_f32_16x16x32_f16 v[90:93], v[198:201], v[218:221], v[90:93]
	s_mov_b32 m0, s88
	v_mfma_f32_16x16x32_f16 v[94:97], v[198:201], v[222:225], v[94:97]
	global_load_lds_dwordx4 v[118:119], off
	v_lshl_add_u64 v[118:119], v[118:119], 0, s[72:73]
	v_mfma_f32_16x16x32_f16 v[34:37], v[198:201], v[226:229], v[34:37]
	s_mov_b32 m0, s89
	v_mfma_f32_16x16x32_f16 v[38:41], v[198:201], v[230:233], v[38:41]
	global_load_lds_dwordx4 v[120:121], off
	v_lshl_add_u64 v[120:121], v[120:121], 0, s[72:73]
	v_mfma_f32_16x16x32_f16 v[82:85], v[202:205], v[218:221], v[82:85]
	s_mov_b32 m0, s90
	v_mfma_f32_16x16x32_f16 v[86:89], v[202:205], v[222:225], v[86:89]
	global_load_lds_dwordx4 v[122:123], off
	v_lshl_add_u64 v[122:123], v[122:123], 0, s[72:73]
	v_mfma_f32_16x16x32_f16 v[18:21], v[202:205], v[226:229], v[18:21]
	s_mov_b32 m0, s91
	v_mfma_f32_16x16x32_f16 v[22:25], v[202:205], v[230:233], v[22:25]
	global_load_lds_dwordx4 v[124:125], off
	v_lshl_add_u64 v[124:125], v[124:125], 0, s[72:73]
	v_mfma_f32_16x16x32_f16 v[74:77], v[206:209], v[218:221], v[74:77]
	ds_read_b128 v[178:181], v236 offset:28672
	v_mfma_f32_16x16x32_f16 v[78:81], v[206:209], v[222:225], v[78:81]
	ds_read_b128 v[186:189], v236 offset:30720
	v_mfma_f32_16x16x32_f16 v[10:13], v[206:209], v[226:229], v[10:13]
	ds_read_b128 v[174:177], v236 offset:32768
	v_mfma_f32_16x16x32_f16 v[14:17], v[206:209], v[230:233], v[14:17]
	ds_read_b128 v[182:185], v236 offset:34816
	v_mfma_f32_16x16x32_f16 v[66:69], v[210:213], v[218:221], v[66:69]
	ds_read_b128 v[146:149], v234
	v_mfma_f32_16x16x32_f16 v[70:73], v[210:213], v[222:225], v[70:73]
	ds_read_b128 v[150:153], v234 offset:2048
	v_mfma_f32_16x16x32_f16 v[2:5], v[210:213], v[226:229], v[2:5]
	ds_read_b128 v[154:157], v234 offset:4096
	v_mfma_f32_16x16x32_f16 v[6:9], v[210:213], v[230:233], v[6:9]
	ds_read_b128 v[158:161], v234 offset:6144
	v_mfma_f32_16x16x32_f16 v[58:61], v[214:217], v[218:221], v[58:61]
	ds_read_b128 v[162:165], v234 offset:8192
	v_mfma_f32_16x16x32_f16 v[62:65], v[214:217], v[222:225], v[62:65]
	ds_read_b128 v[166:169], v234 offset:10240
	v_mfma_f32_16x16x32_f16 v[26:29], v[214:217], v[226:229], v[26:29]
	ds_read_b128 v[170:173], v234 offset:12288
	v_mfma_f32_16x16x32_f16 v[30:33], v[214:217], v[230:233], v[30:33]
	s_waitcnt lgkmcnt(0)
	v_mfma_f32_16x16x32_f16 v[110:113], v[146:149], v[178:181], v[110:113]
	ds_read_b128 v[218:221], v237 offset:28672
	v_mfma_f32_16x16x32_f16 v[106:109], v[146:149], v[186:189], v[106:109]
	ds_read_b128 v[222:225], v237 offset:30720
	v_mfma_f32_16x16x32_f16 v[50:53], v[146:149], v[174:177], v[50:53]
	ds_read_b128 v[226:229], v237 offset:32768
	v_mfma_f32_16x16x32_f16 v[54:57], v[146:149], v[182:185], v[54:57]
	ds_read_b128 v[230:233], v237 offset:34816
	v_mfma_f32_16x16x32_f16 v[98:101], v[150:153], v[178:181], v[98:101]
	ds_read_b128 v[190:193], v235
	v_mfma_f32_16x16x32_f16 v[102:105], v[150:153], v[186:189], v[102:105]
	ds_read_b128 v[194:197], v235 offset:2048
	v_mfma_f32_16x16x32_f16 v[42:45], v[150:153], v[174:177], v[42:45]
	ds_read_b128 v[198:201], v235 offset:4096
	v_mfma_f32_16x16x32_f16 v[46:49], v[150:153], v[182:185], v[46:49]
	ds_read_b128 v[202:205], v235 offset:6144
	v_mfma_f32_16x16x32_f16 v[90:93], v[154:157], v[178:181], v[90:93]
	ds_read_b128 v[206:209], v235 offset:8192
	v_mfma_f32_16x16x32_f16 v[94:97], v[154:157], v[186:189], v[94:97]
	ds_read_b128 v[210:213], v235 offset:10240
	v_mfma_f32_16x16x32_f16 v[34:37], v[154:157], v[174:177], v[34:37]
	ds_read_b128 v[214:217], v235 offset:12288
	v_mfma_f32_16x16x32_f16 v[38:41], v[154:157], v[182:185], v[38:41]
	v_mfma_f32_16x16x32_f16 v[82:85], v[158:161], v[178:181], v[82:85]
	v_mfma_f32_16x16x32_f16 v[86:89], v[158:161], v[186:189], v[86:89]
	v_mfma_f32_16x16x32_f16 v[18:21], v[158:161], v[174:177], v[18:21]
	v_mfma_f32_16x16x32_f16 v[22:25], v[158:161], v[182:185], v[22:25]
	v_mfma_f32_16x16x32_f16 v[74:77], v[162:165], v[178:181], v[74:77]
	v_mfma_f32_16x16x32_f16 v[78:81], v[162:165], v[186:189], v[78:81]
	v_mfma_f32_16x16x32_f16 v[10:13], v[162:165], v[174:177], v[10:13]
	v_mfma_f32_16x16x32_f16 v[14:17], v[162:165], v[182:185], v[14:17]
	v_mfma_f32_16x16x32_f16 v[66:69], v[166:169], v[178:181], v[66:69]
	v_mfma_f32_16x16x32_f16 v[70:73], v[166:169], v[186:189], v[70:73]
	v_mfma_f32_16x16x32_f16 v[2:5], v[166:169], v[174:177], v[2:5]
	v_mfma_f32_16x16x32_f16 v[6:9], v[166:169], v[182:185], v[6:9]
	v_mfma_f32_16x16x32_f16 v[58:61], v[170:173], v[178:181], v[58:61]
	v_mfma_f32_16x16x32_f16 v[62:65], v[170:173], v[186:189], v[62:65]
	v_mfma_f32_16x16x32_f16 v[26:29], v[170:173], v[174:177], v[26:29]
	v_mfma_f32_16x16x32_f16 v[30:33], v[170:173], v[182:185], v[30:33]
	s_waitcnt lgkmcnt(0)
	s_waitcnt vmcnt(0)
	s_barrier
	s_sub_i32 s93, s93, 1
	s_cmp_lg_u32 s93, 0
	s_cbranch_scc1 .Lgp_loop_a
	v_mfma_f32_16x16x32_f16 v[110:113], v[190:193], v[218:221], v[110:113]
	ds_read_b128 v[178:181], v142 offset:28672
	v_mfma_f32_16x16x32_f16 v[106:109], v[190:193], v[222:225], v[106:109]
	ds_read_b128 v[186:189], v142 offset:30720
	v_mfma_f32_16x16x32_f16 v[50:53], v[190:193], v[226:229], v[50:53]
	ds_read_b128 v[174:177], v142 offset:32768
	v_mfma_f32_16x16x32_f16 v[54:57], v[190:193], v[230:233], v[54:57]
	ds_read_b128 v[182:185], v142 offset:34816
	v_mfma_f32_16x16x32_f16 v[98:101], v[194:197], v[218:221], v[98:101]
	ds_read_b128 v[146:149], v140
	v_mfma_f32_16x16x32_f16 v[102:105], v[194:197], v[222:225], v[102:105]
	ds_read_b128 v[150:153], v140 offset:2048
	v_mfma_f32_16x16x32_f16 v[42:45], v[194:197], v[226:229], v[42:45]
	ds_read_b128 v[154:157], v140 offset:4096
	v_mfma_f32_16x16x32_f16 v[46:49], v[194:197], v[230:233], v[46:49]
	ds_read_b128 v[158:161], v140 offset:6144
	v_mfma_f32_16x16x32_f16 v[90:93], v[198:201], v[218:221], v[90:93]
	ds_read_b128 v[162:165], v140 offset:8192
	v_mfma_f32_16x16x32_f16 v[94:97], v[198:201], v[222:225], v[94:97]
	ds_read_b128 v[166:169], v140 offset:10240
	v_mfma_f32_16x16x32_f16 v[34:37], v[198:201], v[226:229], v[34:37]
	ds_read_b128 v[170:173], v140 offset:12288
	v_mfma_f32_16x16x32_f16 v[38:41], v[198:201], v[230:233], v[38:41]
	v_mfma_f32_16x16x32_f16 v[82:85], v[202:205], v[218:221], v[82:85]
	v_mfma_f32_16x16x32_f16 v[86:89], v[202:205], v[222:225], v[86:89]
	v_mfma_f32_16x16x32_f16 v[18:21], v[202:205], v[226:229], v[18:21]
	v_mfma_f32_16x16x32_f16 v[22:25], v[202:205], v[230:233], v[22:25]
	v_mfma_f32_16x16x32_f16 v[74:77], v[206:209], v[218:221], v[74:77]
	v_mfma_f32_16x16x32_f16 v[78:81], v[206:209], v[222:225], v[78:81]
	v_mfma_f32_16x16x32_f16 v[10:13], v[206:209], v[226:229], v[10:13]
	v_mfma_f32_16x16x32_f16 v[14:17], v[206:209], v[230:233], v[14:17]
	v_mfma_f32_16x16x32_f16 v[66:69], v[210:213], v[218:221], v[66:69]
	v_mfma_f32_16x16x32_f16 v[70:73], v[210:213], v[222:225], v[70:73]
	v_mfma_f32_16x16x32_f16 v[2:5], v[210:213], v[226:229], v[2:5]
	v_mfma_f32_16x16x32_f16 v[6:9], v[210:213], v[230:233], v[6:9]
	v_mfma_f32_16x16x32_f16 v[58:61], v[214:217], v[218:221], v[58:61]
	v_mfma_f32_16x16x32_f16 v[62:65], v[214:217], v[222:225], v[62:65]
	v_mfma_f32_16x16x32_f16 v[26:29], v[214:217], v[226:229], v[26:29]
	v_mfma_f32_16x16x32_f16 v[30:33], v[214:217], v[230:233], v[30:33]
	s_waitcnt lgkmcnt(0)
	v_mfma_f32_16x16x32_f16 v[110:113], v[146:149], v[178:181], v[110:113]
	ds_read_b128 v[218:221], v143 offset:28672
	v_mfma_f32_16x16x32_f16 v[106:109], v[146:149], v[186:189], v[106:109]
	ds_read_b128 v[222:225], v143 offset:30720
	v_mfma_f32_16x16x32_f16 v[50:53], v[146:149], v[174:177], v[50:53]
	ds_read_b128 v[226:229], v143 offset:32768
	v_mfma_f32_16x16x32_f16 v[54:57], v[146:149], v[182:185], v[54:57]
	ds_read_b128 v[230:233], v143 offset:34816
	v_mfma_f32_16x16x32_f16 v[98:101], v[150:153], v[178:181], v[98:101]
	ds_read_b128 v[190:193], v141
	v_mfma_f32_16x16x32_f16 v[102:105], v[150:153], v[186:189], v[102:105]
	ds_read_b128 v[194:197], v141 offset:2048
	v_mfma_f32_16x16x32_f16 v[42:45], v[150:153], v[174:177], v[42:45]
	ds_read_b128 v[198:201], v141 offset:4096
	v_mfma_f32_16x16x32_f16 v[46:49], v[150:153], v[182:185], v[46:49]
	ds_read_b128 v[202:205], v141 offset:6144
	v_mfma_f32_16x16x32_f16 v[90:93], v[154:157], v[178:181], v[90:93]
	ds_read_b128 v[206:209], v141 offset:8192
	v_mfma_f32_16x16x32_f16 v[94:97], v[154:157], v[186:189], v[94:97]
	ds_read_b128 v[210:213], v141 offset:10240
	v_mfma_f32_16x16x32_f16 v[34:37], v[154:157], v[174:177], v[34:37]
	ds_read_b128 v[214:217], v141 offset:12288
	v_mfma_f32_16x16x32_f16 v[38:41], v[154:157], v[182:185], v[38:41]
	v_mfma_f32_16x16x32_f16 v[82:85], v[158:161], v[178:181], v[82:85]
	v_mfma_f32_16x16x32_f16 v[86:89], v[158:161], v[186:189], v[86:89]
	v_mfma_f32_16x16x32_f16 v[18:21], v[158:161], v[174:177], v[18:21]
	v_mfma_f32_16x16x32_f16 v[22:25], v[158:161], v[182:185], v[22:25]
	v_mfma_f32_16x16x32_f16 v[74:77], v[162:165], v[178:181], v[74:77]
	v_mfma_f32_16x16x32_f16 v[78:81], v[162:165], v[186:189], v[78:81]
	v_mfma_f32_16x16x32_f16 v[10:13], v[162:165], v[174:177], v[10:13]
	v_mfma_f32_16x16x32_f16 v[14:17], v[162:165], v[182:185], v[14:17]
	v_mfma_f32_16x16x32_f16 v[66:69], v[166:169], v[178:181], v[66:69]
	v_mfma_f32_16x16x32_f16 v[70:73], v[166:169], v[186:189], v[70:73]
	v_mfma_f32_16x16x32_f16 v[2:5], v[166:169], v[174:177], v[2:5]
	v_mfma_f32_16x16x32_f16 v[6:9], v[166:169], v[182:185], v[6:9]
	v_mfma_f32_16x16x32_f16 v[58:61], v[170:173], v[178:181], v[58:61]
	v_mfma_f32_16x16x32_f16 v[62:65], v[170:173], v[186:189], v[62:65]
	v_mfma_f32_16x16x32_f16 v[26:29], v[170:173], v[174:177], v[26:29]
	v_mfma_f32_16x16x32_f16 v[30:33], v[170:173], v[182:185], v[30:33]
	s_waitcnt lgkmcnt(0)
	v_mfma_f32_16x16x32_f16 v[110:113], v[190:193], v[218:221], v[110:113]
	v_mfma_f32_16x16x32_f16 v[106:109], v[190:193], v[222:225], v[106:109]
	v_mfma_f32_16x16x32_f16 v[50:53], v[190:193], v[226:229], v[50:53]
	v_mfma_f32_16x16x32_f16 v[54:57], v[190:193], v[230:233], v[54:57]
	v_mfma_f32_16x16x32_f16 v[98:101], v[194:197], v[218:221], v[98:101]
	v_mfma_f32_16x16x32_f16 v[102:105], v[194:197], v[222:225], v[102:105]
	v_mfma_f32_16x16x32_f16 v[42:45], v[194:197], v[226:229], v[42:45]
	v_mfma_f32_16x16x32_f16 v[46:49], v[194:197], v[230:233], v[46:49]
	v_mfma_f32_16x16x32_f16 v[90:93], v[198:201], v[218:221], v[90:93]
	v_mfma_f32_16x16x32_f16 v[94:97], v[198:201], v[222:225], v[94:97]
	v_mfma_f32_16x16x32_f16 v[34:37], v[198:201], v[226:229], v[34:37]
	v_mfma_f32_16x16x32_f16 v[38:41], v[198:201], v[230:233], v[38:41]
	v_mfma_f32_16x16x32_f16 v[82:85], v[202:205], v[218:221], v[82:85]
	v_mfma_f32_16x16x32_f16 v[86:89], v[202:205], v[222:225], v[86:89]
	v_mfma_f32_16x16x32_f16 v[18:21], v[202:205], v[226:229], v[18:21]
	v_mfma_f32_16x16x32_f16 v[22:25], v[202:205], v[230:233], v[22:25]
	v_mfma_f32_16x16x32_f16 v[74:77], v[206:209], v[218:221], v[74:77]
	v_mfma_f32_16x16x32_f16 v[78:81], v[206:209], v[222:225], v[78:81]
	v_mfma_f32_16x16x32_f16 v[10:13], v[206:209], v[226:229], v[10:13]
	v_mfma_f32_16x16x32_f16 v[14:17], v[206:209], v[230:233], v[14:17]
	v_mfma_f32_16x16x32_f16 v[66:69], v[210:213], v[218:221], v[66:69]
	v_mfma_f32_16x16x32_f16 v[70:73], v[210:213], v[222:225], v[70:73]
	v_mfma_f32_16x16x32_f16 v[2:5], v[210:213], v[226:229], v[2:5]
	v_mfma_f32_16x16x32_f16 v[6:9], v[210:213], v[230:233], v[6:9]
	v_mfma_f32_16x16x32_f16 v[58:61], v[214:217], v[218:221], v[58:61]
	v_mfma_f32_16x16x32_f16 v[62:65], v[214:217], v[222:225], v[62:65]
	v_mfma_f32_16x16x32_f16 v[26:29], v[214:217], v[226:229], v[26:29]
	v_mfma_f32_16x16x32_f16 v[30:33], v[214:217], v[230:233], v[30:33]
	s_branch .LBB5_12
.Lgp_classB:
	.p2alignl 6, 3212836864
